# adaLN modulation GEMV K loop as one rotating pipeline of 48 row loads (no drain between the 4 batches), on top of rope hoist
# speedup vs baseline: 1.0431x; 1.0045x over previous
.LBB0_11:
	s_mul_hi_i32 s10, s14, 0x2aaaaaab
	s_lshr_b32 s11, s10, 31
	s_ashr_i32 s15, s10, 4
	s_add_i32 s15, s15, s11
	s_mul_i32 s10, s15, 0x60
	s_sub_i32 s10, s14, s10
	s_lshl_b32 s10, s10, 6
	s_ashr_i32 s11, s10, 31
	s_mul_i32 s17, s15, 0x1800000
	s_lshl_b64 s[12:13], s[10:11], 2
	s_mul_hi_i32 s16, s15, 0x1800000
	s_add_u32 s12, s17, s12
	s_addc_u32 s13, s16, s13
	v_lshl_add_u64 v[36:37], v[34:35], 0, s[12:13]
	s_movk_i32 s12, 0xffe0
	v_add_co_u32_e32 v136, vcc, 0xfff46000, v36
	s_mov_b64 s[16:17], 0x6000
	v_addc_co_u32_e32 v137, vcc, -1, v37, vcc
	v_mov_b32_e32 v38, 0
	v_mov_b32_e32 v39, v33
	ds_read_b128 v[104:107], v27
	ds_read_b128 v[108:111], v27 offset:16
	ds_read_b128 v[112:115], v27 offset:4096
	ds_read_b128 v[116:119], v27 offset:4112
	global_load_dword v40, v[136:137], off nt
	v_lshl_add_u64 v[136:137], v[136:137], 0, s[16:17]
	global_load_dword v41, v[136:137], off nt
	v_lshl_add_u64 v[136:137], v[136:137], 0, s[16:17]
	global_load_dword v42, v[136:137], off nt
	v_lshl_add_u64 v[136:137], v[136:137], 0, s[16:17]
	global_load_dword v43, v[136:137], off nt
	v_lshl_add_u64 v[136:137], v[136:137], 0, s[16:17]
	global_load_dword v44, v[136:137], off nt
	v_lshl_add_u64 v[136:137], v[136:137], 0, s[16:17]
	global_load_dword v45, v[136:137], off nt
	v_lshl_add_u64 v[136:137], v[136:137], 0, s[16:17]
	global_load_dword v46, v[136:137], off nt
	v_lshl_add_u64 v[136:137], v[136:137], 0, s[16:17]
	global_load_dword v47, v[136:137], off nt
	v_lshl_add_u64 v[136:137], v[136:137], 0, s[16:17]
	global_load_dword v48, v[136:137], off nt
	v_lshl_add_u64 v[136:137], v[136:137], 0, s[16:17]
	global_load_dword v49, v[136:137], off nt
	v_lshl_add_u64 v[136:137], v[136:137], 0, s[16:17]
	global_load_dword v50, v[136:137], off nt
	v_lshl_add_u64 v[136:137], v[136:137], 0, s[16:17]
	global_load_dword v51, v[136:137], off nt
	v_lshl_add_u64 v[136:137], v[136:137], 0, s[16:17]
	global_load_dword v52, v[136:137], off nt
	v_lshl_add_u64 v[136:137], v[136:137], 0, s[16:17]
	global_load_dword v53, v[136:137], off nt
	v_lshl_add_u64 v[136:137], v[136:137], 0, s[16:17]
	global_load_dword v54, v[136:137], off nt
	v_lshl_add_u64 v[136:137], v[136:137], 0, s[16:17]
	global_load_dword v55, v[136:137], off nt
	v_lshl_add_u64 v[136:137], v[136:137], 0, s[16:17]
	global_load_dword v56, v[136:137], off nt
	v_lshl_add_u64 v[136:137], v[136:137], 0, s[16:17]
	global_load_dword v57, v[136:137], off nt
	v_lshl_add_u64 v[136:137], v[136:137], 0, s[16:17]
	global_load_dword v58, v[136:137], off nt
	v_lshl_add_u64 v[136:137], v[136:137], 0, s[16:17]
	global_load_dword v59, v[136:137], off nt
	v_lshl_add_u64 v[136:137], v[136:137], 0, s[16:17]
	global_load_dword v60, v[136:137], off nt
	v_lshl_add_u64 v[136:137], v[136:137], 0, s[16:17]
	global_load_dword v61, v[136:137], off nt
	v_lshl_add_u64 v[136:137], v[136:137], 0, s[16:17]
	global_load_dword v62, v[136:137], off nt
	v_lshl_add_u64 v[136:137], v[136:137], 0, s[16:17]
	global_load_dword v63, v[136:137], off nt
	v_lshl_add_u64 v[136:137], v[136:137], 0, s[16:17]
	global_load_dword v64, v[136:137], off nt
	v_lshl_add_u64 v[136:137], v[136:137], 0, s[16:17]
	global_load_dword v65, v[136:137], off nt
	v_lshl_add_u64 v[136:137], v[136:137], 0, s[16:17]
	global_load_dword v66, v[136:137], off nt
	v_lshl_add_u64 v[136:137], v[136:137], 0, s[16:17]
	global_load_dword v67, v[136:137], off nt
	v_lshl_add_u64 v[136:137], v[136:137], 0, s[16:17]
	global_load_dword v68, v[136:137], off nt
	v_lshl_add_u64 v[136:137], v[136:137], 0, s[16:17]
	global_load_dword v69, v[136:137], off nt
	v_lshl_add_u64 v[136:137], v[136:137], 0, s[16:17]
	global_load_dword v70, v[136:137], off nt
	v_lshl_add_u64 v[136:137], v[136:137], 0, s[16:17]
	global_load_dword v71, v[136:137], off nt
	v_lshl_add_u64 v[136:137], v[136:137], 0, s[16:17]
	global_load_dword v72, v[136:137], off nt
	v_lshl_add_u64 v[136:137], v[136:137], 0, s[16:17]
	global_load_dword v73, v[136:137], off nt
	v_lshl_add_u64 v[136:137], v[136:137], 0, s[16:17]
	global_load_dword v74, v[136:137], off nt
	v_lshl_add_u64 v[136:137], v[136:137], 0, s[16:17]
	global_load_dword v75, v[136:137], off nt
	v_lshl_add_u64 v[136:137], v[136:137], 0, s[16:17]
	global_load_dword v76, v[136:137], off nt
	v_lshl_add_u64 v[136:137], v[136:137], 0, s[16:17]
	global_load_dword v77, v[136:137], off nt
	v_lshl_add_u64 v[136:137], v[136:137], 0, s[16:17]
	global_load_dword v78, v[136:137], off nt
	v_lshl_add_u64 v[136:137], v[136:137], 0, s[16:17]
	global_load_dword v79, v[136:137], off nt
	v_lshl_add_u64 v[136:137], v[136:137], 0, s[16:17]
	global_load_dword v80, v[136:137], off nt
	v_lshl_add_u64 v[136:137], v[136:137], 0, s[16:17]
	global_load_dword v81, v[136:137], off nt
	v_lshl_add_u64 v[136:137], v[136:137], 0, s[16:17]
	global_load_dword v82, v[136:137], off nt
	v_lshl_add_u64 v[136:137], v[136:137], 0, s[16:17]
	global_load_dword v83, v[136:137], off nt
	v_lshl_add_u64 v[136:137], v[136:137], 0, s[16:17]
	global_load_dword v84, v[136:137], off nt
	v_lshl_add_u64 v[136:137], v[136:137], 0, s[16:17]
	global_load_dword v85, v[136:137], off nt
	v_lshl_add_u64 v[136:137], v[136:137], 0, s[16:17]
	global_load_dword v86, v[136:137], off nt
	v_lshl_add_u64 v[136:137], v[136:137], 0, s[16:17]
	global_load_dword v87, v[136:137], off nt
	v_lshl_add_u64 v[136:137], v[136:137], 0, s[16:17]
	ds_read_b128 v[120:123], v27 offset:32
	ds_read_b128 v[124:127], v27 offset:48
	ds_read_b128 v[128:131], v27 offset:4128
	ds_read_b128 v[132:135], v27 offset:4144
	s_waitcnt lgkmcnt(4)
	s_waitcnt vmcnt(47)
	v_fma_f32 v38, v40, v104, v38
	v_fma_f32 v39, v40, v112, v39
	global_load_dword v40, v[136:137], off nt
	v_lshl_add_u64 v[136:137], v[136:137], 0, s[16:17]
	s_waitcnt vmcnt(47)
	v_fma_f32 v38, v41, v105, v38
	v_fma_f32 v39, v41, v113, v39
	global_load_dword v41, v[136:137], off nt
	v_lshl_add_u64 v[136:137], v[136:137], 0, s[16:17]
	s_waitcnt vmcnt(47)
	v_fma_f32 v38, v42, v106, v38
	v_fma_f32 v39, v42, v114, v39
	global_load_dword v42, v[136:137], off nt
	v_lshl_add_u64 v[136:137], v[136:137], 0, s[16:17]
	s_waitcnt vmcnt(47)
	v_fma_f32 v38, v43, v107, v38
	v_fma_f32 v39, v43, v115, v39
	global_load_dword v43, v[136:137], off nt
	v_lshl_add_u64 v[136:137], v[136:137], 0, s[16:17]
	s_waitcnt vmcnt(47)
	v_fma_f32 v38, v44, v108, v38
	v_fma_f32 v39, v44, v116, v39
	global_load_dword v44, v[136:137], off nt
	v_lshl_add_u64 v[136:137], v[136:137], 0, s[16:17]
	s_waitcnt vmcnt(47)
	v_fma_f32 v38, v45, v109, v38
	v_fma_f32 v39, v45, v117, v39
	global_load_dword v45, v[136:137], off nt
	v_lshl_add_u64 v[136:137], v[136:137], 0, s[16:17]
	s_waitcnt vmcnt(47)
	v_fma_f32 v38, v46, v110, v38
	v_fma_f32 v39, v46, v118, v39
	global_load_dword v46, v[136:137], off nt
	v_lshl_add_u64 v[136:137], v[136:137], 0, s[16:17]
	s_waitcnt vmcnt(47)
	v_fma_f32 v38, v47, v111, v38
	v_fma_f32 v39, v47, v119, v39
	global_load_dword v47, v[136:137], off nt
	v_lshl_add_u64 v[136:137], v[136:137], 0, s[16:17]
	ds_read_b128 v[104:107], v27 offset:64
	ds_read_b128 v[108:111], v27 offset:80
	ds_read_b128 v[112:115], v27 offset:4160
	ds_read_b128 v[116:119], v27 offset:4176
	s_waitcnt lgkmcnt(4)
	s_waitcnt vmcnt(47)
	v_fma_f32 v38, v48, v120, v38
	v_fma_f32 v39, v48, v128, v39
	global_load_dword v48, v[136:137], off nt
	v_lshl_add_u64 v[136:137], v[136:137], 0, s[16:17]
	s_waitcnt vmcnt(47)
	v_fma_f32 v38, v49, v121, v38
	v_fma_f32 v39, v49, v129, v39
	global_load_dword v49, v[136:137], off nt
	v_lshl_add_u64 v[136:137], v[136:137], 0, s[16:17]
	s_waitcnt vmcnt(47)
	v_fma_f32 v38, v50, v122, v38
	v_fma_f32 v39, v50, v130, v39
	global_load_dword v50, v[136:137], off nt
	v_lshl_add_u64 v[136:137], v[136:137], 0, s[16:17]
	s_waitcnt vmcnt(47)
	v_fma_f32 v38, v51, v123, v38
	v_fma_f32 v39, v51, v131, v39
	global_load_dword v51, v[136:137], off nt
	v_lshl_add_u64 v[136:137], v[136:137], 0, s[16:17]
	s_waitcnt vmcnt(47)
	v_fma_f32 v38, v52, v124, v38
	v_fma_f32 v39, v52, v132, v39
	global_load_dword v52, v[136:137], off nt
	v_lshl_add_u64 v[136:137], v[136:137], 0, s[16:17]
	s_waitcnt vmcnt(47)
	v_fma_f32 v38, v53, v125, v38
	v_fma_f32 v39, v53, v133, v39
	global_load_dword v53, v[136:137], off nt
	v_lshl_add_u64 v[136:137], v[136:137], 0, s[16:17]
	s_waitcnt vmcnt(47)
	v_fma_f32 v38, v54, v126, v38
	v_fma_f32 v39, v54, v134, v39
	global_load_dword v54, v[136:137], off nt
	v_lshl_add_u64 v[136:137], v[136:137], 0, s[16:17]
	s_waitcnt vmcnt(47)
	v_fma_f32 v38, v55, v127, v38
	v_fma_f32 v39, v55, v135, v39
	global_load_dword v55, v[136:137], off nt
	v_lshl_add_u64 v[136:137], v[136:137], 0, s[16:17]
	ds_read_b128 v[120:123], v27 offset:96
	ds_read_b128 v[124:127], v27 offset:112
	ds_read_b128 v[128:131], v27 offset:4192
	ds_read_b128 v[132:135], v27 offset:4208
	s_waitcnt lgkmcnt(4)
	s_waitcnt vmcnt(47)
	v_fma_f32 v38, v56, v104, v38
	v_fma_f32 v39, v56, v112, v39
	global_load_dword v56, v[136:137], off nt
	v_lshl_add_u64 v[136:137], v[136:137], 0, s[16:17]
	s_waitcnt vmcnt(47)
	v_fma_f32 v38, v57, v105, v38
	v_fma_f32 v39, v57, v113, v39
	global_load_dword v57, v[136:137], off nt
	v_lshl_add_u64 v[136:137], v[136:137], 0, s[16:17]
	s_waitcnt vmcnt(47)
	v_fma_f32 v38, v58, v106, v38
	v_fma_f32 v39, v58, v114, v39
	global_load_dword v58, v[136:137], off nt
	v_lshl_add_u64 v[136:137], v[136:137], 0, s[16:17]
	s_waitcnt vmcnt(47)
	v_fma_f32 v38, v59, v107, v38
	v_fma_f32 v39, v59, v115, v39
	global_load_dword v59, v[136:137], off nt
	v_lshl_add_u64 v[136:137], v[136:137], 0, s[16:17]
	s_waitcnt vmcnt(47)
	v_fma_f32 v38, v60, v108, v38
	v_fma_f32 v39, v60, v116, v39
	global_load_dword v60, v[136:137], off nt
	v_lshl_add_u64 v[136:137], v[136:137], 0, s[16:17]
	s_waitcnt vmcnt(47)
	v_fma_f32 v38, v61, v109, v38
	v_fma_f32 v39, v61, v117, v39
	global_load_dword v61, v[136:137], off nt
	v_lshl_add_u64 v[136:137], v[136:137], 0, s[16:17]
	s_waitcnt vmcnt(47)
	v_fma_f32 v38, v62, v110, v38
	v_fma_f32 v39, v62, v118, v39
	global_load_dword v62, v[136:137], off nt
	v_lshl_add_u64 v[136:137], v[136:137], 0, s[16:17]
	s_waitcnt vmcnt(47)
	v_fma_f32 v38, v63, v111, v38
	v_fma_f32 v39, v63, v119, v39
	global_load_dword v63, v[136:137], off nt
	v_lshl_add_u64 v[136:137], v[136:137], 0, s[16:17]
	ds_read_b128 v[104:107], v27 offset:128
	ds_read_b128 v[108:111], v27 offset:144
	ds_read_b128 v[112:115], v27 offset:4224
	ds_read_b128 v[116:119], v27 offset:4240
	s_waitcnt lgkmcnt(4)
	s_waitcnt vmcnt(47)
	v_fma_f32 v38, v64, v120, v38
	v_fma_f32 v39, v64, v128, v39
	global_load_dword v64, v[136:137], off nt
	v_lshl_add_u64 v[136:137], v[136:137], 0, s[16:17]
	s_waitcnt vmcnt(47)
	v_fma_f32 v38, v65, v121, v38
	v_fma_f32 v39, v65, v129, v39
	global_load_dword v65, v[136:137], off nt
	v_lshl_add_u64 v[136:137], v[136:137], 0, s[16:17]
	s_waitcnt vmcnt(47)
	v_fma_f32 v38, v66, v122, v38
	v_fma_f32 v39, v66, v130, v39
	global_load_dword v66, v[136:137], off nt
	v_lshl_add_u64 v[136:137], v[136:137], 0, s[16:17]
	s_waitcnt vmcnt(47)
	v_fma_f32 v38, v67, v123, v38
	v_fma_f32 v39, v67, v131, v39
	global_load_dword v67, v[136:137], off nt
	v_lshl_add_u64 v[136:137], v[136:137], 0, s[16:17]
	s_waitcnt vmcnt(47)
	v_fma_f32 v38, v68, v124, v38
	v_fma_f32 v39, v68, v132, v39
	global_load_dword v68, v[136:137], off nt
	v_lshl_add_u64 v[136:137], v[136:137], 0, s[16:17]
	s_waitcnt vmcnt(47)
	v_fma_f32 v38, v69, v125, v38
	v_fma_f32 v39, v69, v133, v39
	global_load_dword v69, v[136:137], off nt
	v_lshl_add_u64 v[136:137], v[136:137], 0, s[16:17]
	s_waitcnt vmcnt(47)
	v_fma_f32 v38, v70, v126, v38
	v_fma_f32 v39, v70, v134, v39
	global_load_dword v70, v[136:137], off nt
	v_lshl_add_u64 v[136:137], v[136:137], 0, s[16:17]
	s_waitcnt vmcnt(47)
	v_fma_f32 v38, v71, v127, v38
	v_fma_f32 v39, v71, v135, v39
	global_load_dword v71, v[136:137], off nt
	v_lshl_add_u64 v[136:137], v[136:137], 0, s[16:17]
	ds_read_b128 v[120:123], v27 offset:160
	ds_read_b128 v[124:127], v27 offset:176
	ds_read_b128 v[128:131], v27 offset:4256
	ds_read_b128 v[132:135], v27 offset:4272
	s_waitcnt lgkmcnt(4)
	s_waitcnt vmcnt(47)
	v_fma_f32 v38, v72, v104, v38
	v_fma_f32 v39, v72, v112, v39
	global_load_dword v72, v[136:137], off nt
	v_lshl_add_u64 v[136:137], v[136:137], 0, s[16:17]
	s_waitcnt vmcnt(47)
	v_fma_f32 v38, v73, v105, v38
	v_fma_f32 v39, v73, v113, v39
	global_load_dword v73, v[136:137], off nt
	v_lshl_add_u64 v[136:137], v[136:137], 0, s[16:17]
	s_waitcnt vmcnt(47)
	v_fma_f32 v38, v74, v106, v38
	v_fma_f32 v39, v74, v114, v39
	global_load_dword v74, v[136:137], off nt
	v_lshl_add_u64 v[136:137], v[136:137], 0, s[16:17]
	s_waitcnt vmcnt(47)
	v_fma_f32 v38, v75, v107, v38
	v_fma_f32 v39, v75, v115, v39
	global_load_dword v75, v[136:137], off nt
	v_lshl_add_u64 v[136:137], v[136:137], 0, s[16:17]
	s_waitcnt vmcnt(47)
	v_fma_f32 v38, v76, v108, v38
	v_fma_f32 v39, v76, v116, v39
	global_load_dword v76, v[136:137], off nt
	v_lshl_add_u64 v[136:137], v[136:137], 0, s[16:17]
	s_waitcnt vmcnt(47)
	v_fma_f32 v38, v77, v109, v38
	v_fma_f32 v39, v77, v117, v39
	global_load_dword v77, v[136:137], off nt
	v_lshl_add_u64 v[136:137], v[136:137], 0, s[16:17]
	s_waitcnt vmcnt(47)
	v_fma_f32 v38, v78, v110, v38
	v_fma_f32 v39, v78, v118, v39
	global_load_dword v78, v[136:137], off nt
	v_lshl_add_u64 v[136:137], v[136:137], 0, s[16:17]
	s_waitcnt vmcnt(47)
	v_fma_f32 v38, v79, v111, v38
	v_fma_f32 v39, v79, v119, v39
	global_load_dword v79, v[136:137], off nt
	v_lshl_add_u64 v[136:137], v[136:137], 0, s[16:17]
	ds_read_b128 v[104:107], v27 offset:192
	ds_read_b128 v[108:111], v27 offset:208
	ds_read_b128 v[112:115], v27 offset:4288
	ds_read_b128 v[116:119], v27 offset:4304
	s_waitcnt lgkmcnt(4)
	s_waitcnt vmcnt(47)
	v_fma_f32 v38, v80, v120, v38
	v_fma_f32 v39, v80, v128, v39
	global_load_dword v80, v[136:137], off nt
	v_lshl_add_u64 v[136:137], v[136:137], 0, s[16:17]
	s_waitcnt vmcnt(47)
	v_fma_f32 v38, v81, v121, v38
	v_fma_f32 v39, v81, v129, v39
	global_load_dword v81, v[136:137], off nt
	v_lshl_add_u64 v[136:137], v[136:137], 0, s[16:17]
	s_waitcnt vmcnt(47)
	v_fma_f32 v38, v82, v122, v38
	v_fma_f32 v39, v82, v130, v39
	global_load_dword v82, v[136:137], off nt
	v_lshl_add_u64 v[136:137], v[136:137], 0, s[16:17]
	s_waitcnt vmcnt(47)
	v_fma_f32 v38, v83, v123, v38
	v_fma_f32 v39, v83, v131, v39
	global_load_dword v83, v[136:137], off nt
	v_lshl_add_u64 v[136:137], v[136:137], 0, s[16:17]
	s_waitcnt vmcnt(47)
	v_fma_f32 v38, v84, v124, v38
	v_fma_f32 v39, v84, v132, v39
	global_load_dword v84, v[136:137], off nt
	v_lshl_add_u64 v[136:137], v[136:137], 0, s[16:17]
	s_waitcnt vmcnt(47)
	v_fma_f32 v38, v85, v125, v38
	v_fma_f32 v39, v85, v133, v39
	global_load_dword v85, v[136:137], off nt
	v_lshl_add_u64 v[136:137], v[136:137], 0, s[16:17]
	s_waitcnt vmcnt(47)
	v_fma_f32 v38, v86, v126, v38
	v_fma_f32 v39, v86, v134, v39
	global_load_dword v86, v[136:137], off nt
	v_lshl_add_u64 v[136:137], v[136:137], 0, s[16:17]
	s_waitcnt vmcnt(47)
	v_fma_f32 v38, v87, v127, v38
	v_fma_f32 v39, v87, v135, v39
	global_load_dword v87, v[136:137], off nt
	v_lshl_add_u64 v[136:137], v[136:137], 0, s[16:17]
	ds_read_b128 v[120:123], v27 offset:224
	ds_read_b128 v[124:127], v27 offset:240
	ds_read_b128 v[128:131], v27 offset:4320
	ds_read_b128 v[132:135], v27 offset:4336
	s_waitcnt lgkmcnt(4)
	s_waitcnt vmcnt(47)
	v_fma_f32 v38, v40, v104, v38
	v_fma_f32 v39, v40, v112, v39
	global_load_dword v40, v[136:137], off nt
	v_lshl_add_u64 v[136:137], v[136:137], 0, s[16:17]
	s_waitcnt vmcnt(47)
	v_fma_f32 v38, v41, v105, v38
	v_fma_f32 v39, v41, v113, v39
	global_load_dword v41, v[136:137], off nt
	v_lshl_add_u64 v[136:137], v[136:137], 0, s[16:17]
	s_waitcnt vmcnt(47)
	v_fma_f32 v38, v42, v106, v38
	v_fma_f32 v39, v42, v114, v39
	global_load_dword v42, v[136:137], off nt
	v_lshl_add_u64 v[136:137], v[136:137], 0, s[16:17]
	s_waitcnt vmcnt(47)
	v_fma_f32 v38, v43, v107, v38
	v_fma_f32 v39, v43, v115, v39
	global_load_dword v43, v[136:137], off nt
	v_lshl_add_u64 v[136:137], v[136:137], 0, s[16:17]
	s_waitcnt vmcnt(47)
	v_fma_f32 v38, v44, v108, v38
	v_fma_f32 v39, v44, v116, v39
	global_load_dword v44, v[136:137], off nt
	v_lshl_add_u64 v[136:137], v[136:137], 0, s[16:17]
	s_waitcnt vmcnt(47)
	v_fma_f32 v38, v45, v109, v38
	v_fma_f32 v39, v45, v117, v39
	global_load_dword v45, v[136:137], off nt
	v_lshl_add_u64 v[136:137], v[136:137], 0, s[16:17]
	s_waitcnt vmcnt(47)
	v_fma_f32 v38, v46, v110, v38
	v_fma_f32 v39, v46, v118, v39
	global_load_dword v46, v[136:137], off nt
	v_lshl_add_u64 v[136:137], v[136:137], 0, s[16:17]
	s_waitcnt vmcnt(47)
	v_fma_f32 v38, v47, v111, v38
	v_fma_f32 v39, v47, v119, v39
	global_load_dword v47, v[136:137], off nt
	v_lshl_add_u64 v[136:137], v[136:137], 0, s[16:17]
	ds_read_b128 v[104:107], v27 offset:256
	ds_read_b128 v[108:111], v27 offset:272
	ds_read_b128 v[112:115], v27 offset:4352
	ds_read_b128 v[116:119], v27 offset:4368
	s_waitcnt lgkmcnt(4)
	s_waitcnt vmcnt(47)
	v_fma_f32 v38, v48, v120, v38
	v_fma_f32 v39, v48, v128, v39
	global_load_dword v48, v[136:137], off nt
	v_lshl_add_u64 v[136:137], v[136:137], 0, s[16:17]
	s_waitcnt vmcnt(47)
	v_fma_f32 v38, v49, v121, v38
	v_fma_f32 v39, v49, v129, v39
	global_load_dword v49, v[136:137], off nt
	v_lshl_add_u64 v[136:137], v[136:137], 0, s[16:17]
	s_waitcnt vmcnt(47)
	v_fma_f32 v38, v50, v122, v38
	v_fma_f32 v39, v50, v130, v39
	global_load_dword v50, v[136:137], off nt
	v_lshl_add_u64 v[136:137], v[136:137], 0, s[16:17]
	s_waitcnt vmcnt(47)
	v_fma_f32 v38, v51, v123, v38
	v_fma_f32 v39, v51, v131, v39
	global_load_dword v51, v[136:137], off nt
	v_lshl_add_u64 v[136:137], v[136:137], 0, s[16:17]
	s_waitcnt vmcnt(47)
	v_fma_f32 v38, v52, v124, v38
	v_fma_f32 v39, v52, v132, v39
	global_load_dword v52, v[136:137], off nt
	v_lshl_add_u64 v[136:137], v[136:137], 0, s[16:17]
	s_waitcnt vmcnt(47)
	v_fma_f32 v38, v53, v125, v38
	v_fma_f32 v39, v53, v133, v39
	global_load_dword v53, v[136:137], off nt
	v_lshl_add_u64 v[136:137], v[136:137], 0, s[16:17]
	s_waitcnt vmcnt(47)
	v_fma_f32 v38, v54, v126, v38
	v_fma_f32 v39, v54, v134, v39
	global_load_dword v54, v[136:137], off nt
	v_lshl_add_u64 v[136:137], v[136:137], 0, s[16:17]
	s_waitcnt vmcnt(47)
	v_fma_f32 v38, v55, v127, v38
	v_fma_f32 v39, v55, v135, v39
	global_load_dword v55, v[136:137], off nt
	v_lshl_add_u64 v[136:137], v[136:137], 0, s[16:17]
	ds_read_b128 v[120:123], v27 offset:288
	ds_read_b128 v[124:127], v27 offset:304
	ds_read_b128 v[128:131], v27 offset:4384
	ds_read_b128 v[132:135], v27 offset:4400
	s_waitcnt lgkmcnt(4)
	s_waitcnt vmcnt(47)
	v_fma_f32 v38, v56, v104, v38
	v_fma_f32 v39, v56, v112, v39
	global_load_dword v56, v[136:137], off nt
	v_lshl_add_u64 v[136:137], v[136:137], 0, s[16:17]
	s_waitcnt vmcnt(47)
	v_fma_f32 v38, v57, v105, v38
	v_fma_f32 v39, v57, v113, v39
	global_load_dword v57, v[136:137], off nt
	v_lshl_add_u64 v[136:137], v[136:137], 0, s[16:17]
	s_waitcnt vmcnt(47)
	v_fma_f32 v38, v58, v106, v38
	v_fma_f32 v39, v58, v114, v39
	global_load_dword v58, v[136:137], off nt
	v_lshl_add_u64 v[136:137], v[136:137], 0, s[16:17]
	s_waitcnt vmcnt(47)
	v_fma_f32 v38, v59, v107, v38
	v_fma_f32 v39, v59, v115, v39
	global_load_dword v59, v[136:137], off nt
	v_lshl_add_u64 v[136:137], v[136:137], 0, s[16:17]
	s_waitcnt vmcnt(47)
	v_fma_f32 v38, v60, v108, v38
	v_fma_f32 v39, v60, v116, v39
	global_load_dword v60, v[136:137], off nt
	v_lshl_add_u64 v[136:137], v[136:137], 0, s[16:17]
	s_waitcnt vmcnt(47)
	v_fma_f32 v38, v61, v109, v38
	v_fma_f32 v39, v61, v117, v39
	global_load_dword v61, v[136:137], off nt
	v_lshl_add_u64 v[136:137], v[136:137], 0, s[16:17]
	s_waitcnt vmcnt(47)
	v_fma_f32 v38, v62, v110, v38
	v_fma_f32 v39, v62, v118, v39
	global_load_dword v62, v[136:137], off nt
	v_lshl_add_u64 v[136:137], v[136:137], 0, s[16:17]
	s_waitcnt vmcnt(47)
	v_fma_f32 v38, v63, v111, v38
	v_fma_f32 v39, v63, v119, v39
	global_load_dword v63, v[136:137], off nt
	v_lshl_add_u64 v[136:137], v[136:137], 0, s[16:17]
	ds_read_b128 v[104:107], v27 offset:320
	ds_read_b128 v[108:111], v27 offset:336
	ds_read_b128 v[112:115], v27 offset:4416
	ds_read_b128 v[116:119], v27 offset:4432
	s_waitcnt lgkmcnt(4)
	s_waitcnt vmcnt(47)
	v_fma_f32 v38, v64, v120, v38
	v_fma_f32 v39, v64, v128, v39
	global_load_dword v64, v[136:137], off nt
	v_lshl_add_u64 v[136:137], v[136:137], 0, s[16:17]
	s_waitcnt vmcnt(47)
	v_fma_f32 v38, v65, v121, v38
	v_fma_f32 v39, v65, v129, v39
	global_load_dword v65, v[136:137], off nt
	v_lshl_add_u64 v[136:137], v[136:137], 0, s[16:17]
	s_waitcnt vmcnt(47)
	v_fma_f32 v38, v66, v122, v38
	v_fma_f32 v39, v66, v130, v39
	global_load_dword v66, v[136:137], off nt
	v_lshl_add_u64 v[136:137], v[136:137], 0, s[16:17]
	s_waitcnt vmcnt(47)
	v_fma_f32 v38, v67, v123, v38
	v_fma_f32 v39, v67, v131, v39
	global_load_dword v67, v[136:137], off nt
	v_lshl_add_u64 v[136:137], v[136:137], 0, s[16:17]
	s_waitcnt vmcnt(47)
	v_fma_f32 v38, v68, v124, v38
	v_fma_f32 v39, v68, v132, v39
	global_load_dword v68, v[136:137], off nt
	v_lshl_add_u64 v[136:137], v[136:137], 0, s[16:17]
	s_waitcnt vmcnt(47)
	v_fma_f32 v38, v69, v125, v38
	v_fma_f32 v39, v69, v133, v39
	global_load_dword v69, v[136:137], off nt
	v_lshl_add_u64 v[136:137], v[136:137], 0, s[16:17]
	s_waitcnt vmcnt(47)
	v_fma_f32 v38, v70, v126, v38
	v_fma_f32 v39, v70, v134, v39
	global_load_dword v70, v[136:137], off nt
	v_lshl_add_u64 v[136:137], v[136:137], 0, s[16:17]
	s_waitcnt vmcnt(47)
	v_fma_f32 v38, v71, v127, v38
	v_fma_f32 v39, v71, v135, v39
	global_load_dword v71, v[136:137], off nt
	ds_read_b128 v[120:123], v27 offset:352
	ds_read_b128 v[124:127], v27 offset:368
	ds_read_b128 v[128:131], v27 offset:4448
	ds_read_b128 v[132:135], v27 offset:4464
	s_waitcnt lgkmcnt(4)
	s_waitcnt vmcnt(47)
	v_fma_f32 v38, v72, v104, v38
	v_fma_f32 v39, v72, v112, v39
	s_waitcnt vmcnt(46)
	v_fma_f32 v38, v73, v105, v38
	v_fma_f32 v39, v73, v113, v39
	s_waitcnt vmcnt(45)
	v_fma_f32 v38, v74, v106, v38
	v_fma_f32 v39, v74, v114, v39
	s_waitcnt vmcnt(44)
	v_fma_f32 v38, v75, v107, v38
	v_fma_f32 v39, v75, v115, v39
	s_waitcnt vmcnt(43)
	v_fma_f32 v38, v76, v108, v38
	v_fma_f32 v39, v76, v116, v39
	s_waitcnt vmcnt(42)
	v_fma_f32 v38, v77, v109, v38
	v_fma_f32 v39, v77, v117, v39
	s_waitcnt vmcnt(41)
	v_fma_f32 v38, v78, v110, v38
	v_fma_f32 v39, v78, v118, v39
	s_waitcnt vmcnt(40)
	v_fma_f32 v38, v79, v111, v38
	v_fma_f32 v39, v79, v119, v39
	ds_read_b128 v[104:107], v27 offset:384
	ds_read_b128 v[108:111], v27 offset:400
	ds_read_b128 v[112:115], v27 offset:4480
	ds_read_b128 v[116:119], v27 offset:4496
	s_waitcnt lgkmcnt(4)
	s_waitcnt vmcnt(39)
	v_fma_f32 v38, v80, v120, v38
	v_fma_f32 v39, v80, v128, v39
	s_waitcnt vmcnt(38)
	v_fma_f32 v38, v81, v121, v38
	v_fma_f32 v39, v81, v129, v39
	s_waitcnt vmcnt(37)
	v_fma_f32 v38, v82, v122, v38
	v_fma_f32 v39, v82, v130, v39
	s_waitcnt vmcnt(36)
	v_fma_f32 v38, v83, v123, v38
	v_fma_f32 v39, v83, v131, v39
	s_waitcnt vmcnt(35)
	v_fma_f32 v38, v84, v124, v38
	v_fma_f32 v39, v84, v132, v39
	s_waitcnt vmcnt(34)
	v_fma_f32 v38, v85, v125, v38
	v_fma_f32 v39, v85, v133, v39
	s_waitcnt vmcnt(33)
	v_fma_f32 v38, v86, v126, v38
	v_fma_f32 v39, v86, v134, v39
	s_waitcnt vmcnt(32)
	v_fma_f32 v38, v87, v127, v38
	v_fma_f32 v39, v87, v135, v39
	ds_read_b128 v[120:123], v27 offset:416
	ds_read_b128 v[124:127], v27 offset:432
	ds_read_b128 v[128:131], v27 offset:4512
	ds_read_b128 v[132:135], v27 offset:4528
	s_waitcnt lgkmcnt(4)
	s_waitcnt vmcnt(31)
	v_fma_f32 v38, v40, v104, v38
	v_fma_f32 v39, v40, v112, v39
	s_waitcnt vmcnt(30)
	v_fma_f32 v38, v41, v105, v38
	v_fma_f32 v39, v41, v113, v39
	s_waitcnt vmcnt(29)
	v_fma_f32 v38, v42, v106, v38
	v_fma_f32 v39, v42, v114, v39
	s_waitcnt vmcnt(28)
	v_fma_f32 v38, v43, v107, v38
	v_fma_f32 v39, v43, v115, v39
	s_waitcnt vmcnt(27)
	v_fma_f32 v38, v44, v108, v38
	v_fma_f32 v39, v44, v116, v39
	s_waitcnt vmcnt(26)
	v_fma_f32 v38, v45, v109, v38
	v_fma_f32 v39, v45, v117, v39
	s_waitcnt vmcnt(25)
	v_fma_f32 v38, v46, v110, v38
	v_fma_f32 v39, v46, v118, v39
	s_waitcnt vmcnt(24)
	v_fma_f32 v38, v47, v111, v38
	v_fma_f32 v39, v47, v119, v39
	ds_read_b128 v[104:107], v27 offset:448
	ds_read_b128 v[108:111], v27 offset:464
	ds_read_b128 v[112:115], v27 offset:4544
	ds_read_b128 v[116:119], v27 offset:4560
	s_waitcnt lgkmcnt(4)
	s_waitcnt vmcnt(23)
	v_fma_f32 v38, v48, v120, v38
	v_fma_f32 v39, v48, v128, v39
	s_waitcnt vmcnt(22)
	v_fma_f32 v38, v49, v121, v38
	v_fma_f32 v39, v49, v129, v39
	s_waitcnt vmcnt(21)
	v_fma_f32 v38, v50, v122, v38
	v_fma_f32 v39, v50, v130, v39
	s_waitcnt vmcnt(20)
	v_fma_f32 v38, v51, v123, v38
	v_fma_f32 v39, v51, v131, v39
	s_waitcnt vmcnt(19)
	v_fma_f32 v38, v52, v124, v38
	v_fma_f32 v39, v52, v132, v39
	s_waitcnt vmcnt(18)
	v_fma_f32 v38, v53, v125, v38
	v_fma_f32 v39, v53, v133, v39
	s_waitcnt vmcnt(17)
	v_fma_f32 v38, v54, v126, v38
	v_fma_f32 v39, v54, v134, v39
	s_waitcnt vmcnt(16)
	v_fma_f32 v38, v55, v127, v38
	v_fma_f32 v39, v55, v135, v39
	ds_read_b128 v[120:123], v27 offset:480
	ds_read_b128 v[124:127], v27 offset:496
	ds_read_b128 v[128:131], v27 offset:4576
	ds_read_b128 v[132:135], v27 offset:4592
	s_waitcnt lgkmcnt(4)
	s_waitcnt vmcnt(15)
	v_fma_f32 v38, v56, v104, v38
	v_fma_f32 v39, v56, v112, v39
	s_waitcnt vmcnt(14)
	v_fma_f32 v38, v57, v105, v38
	v_fma_f32 v39, v57, v113, v39
	s_waitcnt vmcnt(13)
	v_fma_f32 v38, v58, v106, v38
	v_fma_f32 v39, v58, v114, v39
	s_waitcnt vmcnt(12)
	v_fma_f32 v38, v59, v107, v38
	v_fma_f32 v39, v59, v115, v39
	s_waitcnt vmcnt(11)
	v_fma_f32 v38, v60, v108, v38
	v_fma_f32 v39, v60, v116, v39
	s_waitcnt vmcnt(10)
	v_fma_f32 v38, v61, v109, v38
	v_fma_f32 v39, v61, v117, v39
	s_waitcnt vmcnt(9)
	v_fma_f32 v38, v62, v110, v38
	v_fma_f32 v39, v62, v118, v39
	s_waitcnt vmcnt(8)
	v_fma_f32 v38, v63, v111, v38
	v_fma_f32 v39, v63, v119, v39
	s_waitcnt lgkmcnt(0)
	s_waitcnt vmcnt(7)
	v_fma_f32 v38, v64, v120, v38
	v_fma_f32 v39, v64, v128, v39
	s_waitcnt vmcnt(6)
	v_fma_f32 v38, v65, v121, v38
	v_fma_f32 v39, v65, v129, v39
	s_waitcnt vmcnt(5)
	v_fma_f32 v38, v66, v122, v38
	v_fma_f32 v39, v66, v130, v39
	s_waitcnt vmcnt(4)
	v_fma_f32 v38, v67, v123, v38
	v_fma_f32 v39, v67, v131, v39
	s_waitcnt vmcnt(3)
	v_fma_f32 v38, v68, v124, v38
	v_fma_f32 v39, v68, v132, v39
	s_waitcnt vmcnt(2)
	v_fma_f32 v38, v69, v125, v38
	v_fma_f32 v39, v69, v133, v39
	s_waitcnt vmcnt(1)
	v_fma_f32 v38, v70, v126, v38
	v_fma_f32 v39, v70, v134, v39
	s_waitcnt vmcnt(0)
	v_fma_f32 v38, v71, v127, v38
	v_fma_f32 v39, v71, v135, v39
	ds_write2st64_b32 v29, v38, v39 offset0:32 offset1:33
	s_waitcnt lgkmcnt(0)
	s_barrier
	s_and_saveexec_b64 s[12:13], s[0:1]
	s_cbranch_execz .LBB0_15
	s_mul_i32 s16, s15, 0x1800
	s_add_i32 s16, s16, s10
	v_or_b32_e32 v0, s16, v30
	v_readlane_b32 s48, v249, 2
	v_ashrrev_i32_e32 v1, 31, v0
	v_readlane_b32 s56, v249, 10
	v_readlane_b32 s57, v249, 11
	v_readlane_b32 s49, v249, 3
	v_readlane_b32 s50, v249, 4
	v_lshl_add_u64 v[0:1], v[0:1], 2, s[56:57]
	global_load_dword v6, v[0:1], off
	ds_read2st64_b32 v[0:1], v31 offset0:32 offset1:34
	ds_read2st64_b32 v[2:3], v31 offset0:36 offset1:38
	ds_read2st64_b32 v[4:5], v31 offset0:40 offset1:42
	v_readlane_b32 s51, v249, 5
	v_readlane_b32 s52, v249, 6
	s_waitcnt lgkmcnt(2)
	v_add_f32_e32 v0, 0, v0
	v_add_f32_e32 v7, v0, v1
	ds_read2st64_b32 v[0:1], v31 offset0:44 offset1:46
	s_waitcnt lgkmcnt(2)
	v_add_f32_e32 v2, v7, v2
	v_add_f32_e32 v2, v2, v3
	s_waitcnt lgkmcnt(1)
	v_add_f32_e32 v2, v2, v4
	v_add_f32_e32 v2, v2, v5
	s_waitcnt lgkmcnt(0)
	v_add_f32_e32 v0, v2, v0
	v_add_f32_e32 v2, v0, v1
	v_lshl_add_u32 v3, s15, 1, v23
	v_mov_b64_e32 v[0:1], s[96:97]
	v_mad_i64_i32 v[0:1], s[16:17], v3, s3, v[0:1]
	v_lshl_add_u64 v[0:1], s[10:11], 2, v[0:1]
	v_lshl_add_u64 v[0:1], v[0:1], 0, v[32:33]
	v_readlane_b32 s53, v249, 7
	v_readlane_b32 s54, v249, 8
	v_readlane_b32 s55, v249, 9
	v_readlane_b32 s58, v249, 12
	v_readlane_b32 s59, v249, 13
	v_readlane_b32 s60, v249, 14
	v_readlane_b32 s61, v249, 15
	v_readlane_b32 s62, v249, 16
	v_readlane_b32 s63, v249, 17
	s_waitcnt vmcnt(0)
	v_add_f32_e32 v2, v2, v6
	global_store_dword v[0:1], v2, off sc1
